# code warm-up extended: kernel-start warm-up of P0 code by wave 2 (no wait, destination unused in P0) and a 56 KB window before P2
# baseline (speedup 1.0000x reference)
.LBB0_14:
	v_readlane_b32 s2, v253, 9
	s_cmp_lg_u32 s2, 0x80
	s_cbranch_scc1 .Lcwarm_s
	s_getpc_b64 s[2:3]
	v_mbcnt_lo_u32_b32 v250, -1, 0
	v_mbcnt_hi_u32_b32 v250, -1, v250
	v_lshlrev_b32_e32 v250, 7, v250
	global_load_dword v251, v250, s[2:3]
	v_add_u32_e32 v250, 0x2000, v250
	global_load_dword v251, v250, s[2:3]
	v_add_u32_e32 v250, 0x2000, v250
	global_load_dword v251, v250, s[2:3]

.Lxinvw_1:
	s_cmp_lg_u32 s6, 0x80
	s_cbranch_scc1 .Lcwarm_1
	s_getpc_b64 s[6:7]
	v_mbcnt_lo_u32_b32 v0, -1, 0
	v_mbcnt_hi_u32_b32 v0, -1, v0
	v_lshlrev_b32_e32 v0, 7, v0
	global_load_dword v1, v0, s[6:7]
	v_add_u32_e32 v0, 0x2000, v0
	global_load_dword v1, v0, s[6:7]
	v_add_u32_e32 v0, 0x2000, v0
	global_load_dword v1, v0, s[6:7]
	v_add_u32_e32 v0, 0x2000, v0
	global_load_dword v1, v0, s[6:7]
	v_add_u32_e32 v0, 0x2000, v0
	global_load_dword v1, v0, s[6:7]
	v_add_u32_e32 v0, 0x2000, v0
	global_load_dword v1, v0, s[6:7]
	v_add_u32_e32 v0, 0x2000, v0
	global_load_dword v1, v0, s[6:7]
	s_waitcnt vmcnt(0)
